# attention tile loop: QK^T blocks keep five K fragments in flight (counted lgkmcnt) instead of one LDS round trip per MFMA
# baseline (speedup 1.0000x reference)
; #define LAS __attribute__((address_space(3)))
; #define A3_SB() do { if (!A3_NOSBAR) __builtin_amdgcn_sched_barrier(0); } while (0)
; #define A3_PSM(p_, al_, n, h) a3_psm(p_, m_reg, al_, A3_MASKED(n, h), A3_KB(n, h) - qt, hi)
; #define A3_RESC(al_) do { if (__builtin_amdgcn_ballot_w64((al_) < 1.f) != 0ull) { _Pragma("unroll") for (int d_ = 0; d_ < 4; ++d_) _Pragma("unroll") for (int r_ = 0; r_ < 16; ++r_) o[d_][r_] *= (al_); } } while (0)
; #define A3_PSM(p_, al_, n, h) a3_psm(p_, m_reg, al_, A3_MASKED(n, h), A3_KB(n, h) - qt, hi)
; #define A3_RESC(al_) do { if (__builtin_amdgcn_ballot_w64((al_) < 1.f) != 0ull) { _Pragma("unroll") for (int d_ = 0; d_ < 4; ++d_) _Pragma("unroll") for (int r_ = 0; r_ < 16; ++r_) o[d_][r_] *= (al_); } } while (0)
; __device__ __forceinline__ void a3_qk(f32x16& p, const LAS unsigned char* Kh, const bf16x8 (&qr)[8], int base) {
; #pragma unroll
;     for (int r = 0; r < 16; ++r) p[r] = 0.f;
; #pragma unroll
;     for (int d0 = 0; d0 < 8; ++d0) { const bf16x8 b = *(const LAS bf16x8*)(Kh + (base ^ (32 * d0))); if (A3_PRIO) __builtin_amdgcn_s_setprio(1); p = __builtin_amdgcn_mfma_f32_32x32x16_bf16(b, qr[d0], p, 0, 0, 0); if (A3_PRIO) __builtin_amdgcn_s_setprio(0); }
; }
; __device__ __forceinline__ void attn_stream(Frame& F, const float* sinkl, int u_first, int u_stride, int n_lat, int u_extra) {
;     ...
;             A3_SB(); a3_qk(pE, lds + bc + A3_K, qr, kbase);
;             a3_fsm(pO, alO, l_reg, pf); A3_SB();
;             if (j + 2 < NT) A3S_DMA(cu, j + 2, rb + j + 2); else if (has_next) A3S_DMA(nx, j + 2 - NT, rb + j + 2);
;             a3_pv<1>(o, vb0 + bp, pf); A3_PSM(pE, alE, j, 0);
;             A3_RESC(alE);
.LBB13_540:
	s_add_i32 s4, s95, 0xfffe8000
	s_and_b32 s43, s4, 0x18000
	s_add_i32 s4, s57, s43
	s_waitcnt lgkmcnt(0)
	s_barrier
	v_add_u32_e32 v90, s4, v151
	ds_read_b128 v[66:69], v90 offset:16384
	v_add_u32_e32 v181, s4, v153
	ds_read_b128 v[92:95], v181 offset:16384
	v_add_u32_e32 v182, s4, v154
	ds_read_b128 v[220:223], v182 offset:16384
	v_add_u32_e32 v183, s4, v155
	ds_read_b128 v[224:227], v183 offset:16384
	v_add_u32_e32 v184, s4, v156
	ds_read_b128 v[228:231], v184 offset:16384
	s_add_i32 s44, s7, s89
	s_setprio 1
	s_waitcnt lgkmcnt(4)
	v_mfma_f32_32x32x16_bf16 v[66:81], v[66:69], v[100:103], 0
	v_add_u32_e32 v185, s4, v157
	ds_read_b128 v[242:245], v185 offset:16384
	s_waitcnt lgkmcnt(4)
	v_mfma_f32_32x32x16_bf16 v[66:81], v[92:95], v[104:107], v[66:81]
	v_add_u32_e32 v186, s4, v158
	ds_read_b128 v[92:95], v186 offset:16384
	s_waitcnt lgkmcnt(4)
	v_mfma_f32_32x32x16_bf16 v[66:81], v[220:223], v[108:111], v[66:81]
	v_add_u32_e32 v187, s4, v159
	ds_read_b128 v[220:223], v187 offset:16384
	s_waitcnt lgkmcnt(4)
	v_mfma_f32_32x32x16_bf16 v[66:81], v[224:227], v[112:115], v[66:81]
	s_waitcnt lgkmcnt(3)
	v_mfma_f32_32x32x16_bf16 v[66:81], v[228:231], v[116:119], v[66:81]
	s_waitcnt lgkmcnt(2)
	v_mfma_f32_32x32x16_bf16 v[66:81], v[242:245], v[120:123], v[66:81]
	s_waitcnt lgkmcnt(1)
	v_mfma_f32_32x32x16_bf16 v[66:81], v[92:95], v[124:127], v[66:81]
	s_waitcnt lgkmcnt(0)
	v_mfma_f32_32x32x16_bf16 v[66:81], v[220:223], v[128:131], v[66:81]
	s_setprio 0
	s_cmp_ge_u32 s89, s87
	s_cbranch_scc0 .LBB13_545
	s_mov_b64 s[40:41], 0
	s_and_b64 vcc, exec, s[28:29]
	s_mov_b64 s[4:5], 0
	s_cbranch_vccz .LBB13_543
	s_add_i32 s4, s44, -4
	s_cmp_lt_i32 s4, s72
	s_cselect_b32 s5, 0, s72
	s_cselect_b32 s45, s86, s76
	s_sub_i32 s46, s4, s5
	s_mov_b64 s[4:5], -1
	s_and_b64 vcc, exec, s[40:41]
	s_mov_b64 s[40:41], s[34:35]
	s_cbranch_vccz .LBB13_546
	s_branch .LBB13_544

; #define LAS __attribute__((address_space(3)))
; #define A3_SB() do { if (!A3_NOSBAR) __builtin_amdgcn_sched_barrier(0); } while (0)
; #define A3S_QLOAD(U) do { const int hh_ = U.kvh * 4 + (w >> 1), qt_ = U.t0 + 32 * (w & 1) + r32; const size_t mq_ = U.lat ? (size_t)U.b * SEQ + qt_ : (size_t)ML + U.b * CTX + qt_; \
;         const bf16* qp_ = P + mq_ * INC + OFF_Q + hh_ * HD + 8 * hi; _Pragma("unroll") for (int kk_ = 0; kk_ < 8; ++kk_) qr[kk_] = *(const bf16x8*)(qp_ + 16 * kk_); } while (0)
; __device__ __forceinline__ void a3_qk(f32x16& p, const LAS unsigned char* Kh, const bf16x8 (&qr)[8], int base) {
; #pragma unroll
;     for (int r = 0; r < 16; ++r) p[r] = 0.f;
; #pragma unroll
;     for (int d0 = 0; d0 < 8; ++d0) { const bf16x8 b = *(const LAS bf16x8*)(Kh + (base ^ (32 * d0))); if (A3_PRIO) __builtin_amdgcn_s_setprio(1); p = __builtin_amdgcn_mfma_f32_32x32x16_bf16(b, qr[d0], p, 0, 0, 0); if (A3_PRIO) __builtin_amdgcn_s_setprio(0); }
; }
; __device__ __forceinline__ void attn_stream(Frame& F, const float* sinkl, int u_first, int u_stride, int n_lat, int u_extra) {
;     ...
;             A3_SB(); a3_qk(pO, lds + bc + A3_K + 8192, qr, kbase);
;             if (j == NT - 1 && has_next) A3S_QLOAD(nx);
.LBB13_555:
	ds_read_b128 v[82:85], v90 offset:24576
	ds_read_b128 v[190:193], v181 offset:24576
	ds_read_b128 v[220:223], v182 offset:24576
	ds_read_b128 v[224:227], v183 offset:24576
	ds_read_b128 v[228:231], v184 offset:24576
	s_setprio 1
	s_waitcnt lgkmcnt(4)
	v_mfma_f32_32x32x16_bf16 v[82:97], v[82:85], v[100:103], 0
	ds_read_b128 v[242:245], v185 offset:24576
	s_waitcnt lgkmcnt(4)
	v_mfma_f32_32x32x16_bf16 v[82:97], v[190:193], v[104:107], v[82:97]
	ds_read_b128 v[190:193], v186 offset:24576
	s_waitcnt lgkmcnt(4)
	v_mfma_f32_32x32x16_bf16 v[82:97], v[220:223], v[108:111], v[82:97]
	ds_read_b128 v[220:223], v187 offset:24576
	s_waitcnt lgkmcnt(4)
	v_mfma_f32_32x32x16_bf16 v[82:97], v[224:227], v[112:115], v[82:97]
	s_waitcnt lgkmcnt(3)
	v_mfma_f32_32x32x16_bf16 v[82:97], v[228:231], v[116:119], v[82:97]
	s_waitcnt lgkmcnt(2)
	v_mfma_f32_32x32x16_bf16 v[82:97], v[242:245], v[120:123], v[82:97]
	s_waitcnt lgkmcnt(1)
	v_mfma_f32_32x32x16_bf16 v[82:97], v[190:193], v[124:127], v[82:97]
	s_waitcnt lgkmcnt(0)
	v_mfma_f32_32x32x16_bf16 v[82:97], v[220:223], v[128:131], v[82:97]
	s_setprio 0
	s_cmp_lg_u32 s44, 5
	s_cselect_b64 s[44:45], -1, 0
	s_or_b64 s[36:37], s[36:37], s[44:45]
	s_and_b64 vcc, exec, s[36:37]
	s_cbranch_vccnz .LBB13_557
	global_load_dwordx4 v[100:103], v[148:149], off
	global_load_dwordx4 v[104:107], v[148:149], off offset:32
	global_load_dwordx4 v[108:111], v[148:149], off offset:64
	global_load_dwordx4 v[112:115], v[148:149], off offset:96
	global_load_dwordx4 v[116:119], v[148:149], off offset:128
	global_load_dwordx4 v[120:123], v[148:149], off offset:160
	global_load_dwordx4 v[124:127], v[148:149], off offset:192
	global_load_dwordx4 v[128:131], v[148:149], off offset:224
